# dilated-attention output: packed values and row pointers moved by ds_bpermute so that four neighbouring lanes store 32 contiguous bytes (was 64 separate 8-byte requests per store)
# speedup vs baseline: 1.0297x; 1.0059x over previous
.LBB0_453:
	v_add_u32_e32 v190, 0, v47
	ds_read_b128 v[156:159], v190
	ds_read_b128 v[160:163], v190 offset:4352
	ds_read_b128 v[182:185], v190 offset:64
	ds_read_b128 v[186:189], v190 offset:4416
	v_mov_b32_e32 v180, v164
	v_cmp_le_i32_e64 s[36:37], s69, v229
	s_waitcnt vmcnt(7) lgkmcnt(3)
	v_mfma_f32_16x16x32_bf16 v[164:167], v[156:159], v[72:75], 0
	v_mov_b32_e32 v181, v231
	v_add_u32_e32 v47, 0x2200, v47
	s_waitcnt lgkmcnt(2)
	v_mfma_f32_16x16x32_bf16 v[168:171], v[160:163], v[72:75], 0
	s_waitcnt vmcnt(3)
	v_mfma_f32_16x16x32_bf16 v[156:159], v[156:159], v[84:87], 0
	v_mfma_f32_16x16x32_bf16 v[160:163], v[160:163], v[84:87], 0
	s_waitcnt lgkmcnt(1)
	v_mfma_f32_16x16x32_bf16 v[164:167], v[182:185], v[68:71], v[164:167]
	s_waitcnt lgkmcnt(0)
	v_mfma_f32_16x16x32_bf16 v[168:171], v[186:189], v[68:71], v[168:171]
	s_waitcnt vmcnt(2)
	v_mfma_f32_16x16x32_bf16 v[156:159], v[182:185], v[80:83], v[156:159]
	v_mfma_f32_16x16x32_bf16 v[160:163], v[186:189], v[80:83], v[160:163]
	ds_read_b128 v[182:185], v190 offset:128
	ds_read_b128 v[186:189], v190 offset:4480
	s_waitcnt lgkmcnt(0)
	v_mfma_f32_16x16x32_bf16 v[232:235], v[186:189], v[64:67], v[168:171]
	s_waitcnt vmcnt(1)
	v_mfma_f32_16x16x32_bf16 v[160:163], v[186:189], v[76:79], v[160:163]
	ds_read_b128 v[186:189], v190 offset:192
	ds_read_b128 v[236:239], v190 offset:4544
	v_mfma_f32_16x16x32_bf16 v[164:167], v[182:185], v[64:67], v[164:167]
	v_mfma_f32_16x16x32_bf16 v[182:185], v[182:185], v[76:79], v[156:159]
	s_waitcnt lgkmcnt(0)
	v_mfma_f32_16x16x32_bf16 v[156:159], v[236:239], v[60:63], v[232:235]
	v_mfma_f32_16x16x32_bf16 v[168:171], v[186:189], v[60:63], v[164:167]
	s_waitcnt vmcnt(0)
	v_mfma_f32_16x16x32_bf16 v[164:167], v[186:189], v[88:91], v[182:185]
	s_nop 4
	v_mul_f32_e32 v156, 0x3e0293ee, v156
	v_mul_f32_e32 v168, 0x3e0293ee, v168
	v_mul_f32_e32 v169, 0x3e0293ee, v169
	v_subrev_u32_e32 v182, 19, v229
	v_add_u32_e32 v184, s70, v217
	v_add_u32_e32 v183, -3, v229
	v_cmp_le_i32_e32 vcc, s69, v182
	v_add_u32_e32 v182, 0x70, v184
	v_add_u32_e32 v185, 0x80, v184
	v_cmp_gt_u32_e64 s[24:25], s44, v182
	v_cmp_le_i32_e64 s[22:23], s69, v183
	v_cmp_gt_u32_e64 s[0:1], s44, v185
	s_and_b64 s[24:25], s[24:25], s[22:23]
	v_subrev_u32_e32 v183, 18, v229
	s_and_b64 s[0:1], s[0:1], vcc
	v_cndmask_b32_e64 v156, v226, v156, s[24:25]
	v_add_u32_e32 v185, -2, v229
	v_add_u32_e32 v186, 0x7f, v184
	v_cmp_le_i32_e64 s[24:25], s69, v183
	v_add_u32_e32 v183, 0x6f, v184
	v_cndmask_b32_e64 v168, v226, v168, s[0:1]
	v_cmp_gt_u32_e64 s[0:1], s44, v186
	v_cmp_gt_u32_e64 s[28:29], s44, v183
	v_cmp_le_i32_e64 s[26:27], s69, v185
	s_and_b64 s[0:1], s[0:1], s[24:25]
	s_and_b64 s[28:29], s[28:29], s[26:27]
	v_mul_f32_e32 v157, 0x3e0293ee, v157
	v_cndmask_b32_e64 v183, v226, v169, s[0:1]
	v_cndmask_b32_e64 v157, v226, v157, s[28:29]
	v_max_f32_e32 v182, v168, v156
	v_max_f32_e32 v169, v183, v157
	v_max3_f32 v169, v182, s45, v169
	v_subrev_u32_e32 v182, 17, v229
	v_add_u32_e32 v185, -1, v229
	v_add_u32_e32 v186, 0x7e, v184
	v_cmp_le_i32_e64 s[28:29], s69, v182
	v_add_u32_e32 v182, 0x6e, v184
	v_cmp_gt_u32_e64 s[0:1], s44, v186
	v_cmp_gt_u32_e64 s[34:35], s44, v182
	v_cmp_le_i32_e64 s[30:31], s69, v185
	s_and_b64 s[0:1], s[0:1], s[28:29]
	s_and_b64 s[34:35], s[34:35], s[30:31]
	v_mul_f32_e32 v170, 0x3e0293ee, v170
	v_mul_f32_e32 v158, 0x3e0293ee, v158
	v_add_u32_e32 v185, -16, v229
	v_add_u32_e32 v186, 0x7d, v184
	v_add_u32_e32 v184, 0x6d, v184
	v_cndmask_b32_e64 v170, v226, v170, s[0:1]
	v_cndmask_b32_e64 v158, v226, v158, s[34:35]
	v_cmp_gt_u32_e64 s[0:1], s44, v186
	v_cmp_le_i32_e64 s[34:35], s69, v185
	v_cmp_gt_u32_e64 s[40:41], s44, v184
	s_and_b64 s[0:1], s[0:1], s[34:35]
	s_and_b64 s[40:41], s[40:41], s[36:37]
	v_mul_f32_e32 v171, 0x3e0293ee, v171
	v_mul_f32_e32 v159, 0x3e0293ee, v159
	v_cndmask_b32_e64 v184, v226, v171, s[0:1]
	v_cndmask_b32_e64 v159, v226, v159, s[40:41]
	v_max_f32_e32 v182, v170, v158
	v_max_f32_e32 v171, v184, v159
	v_max3_f32 v169, v169, v182, v171
	ds_bpermute_b32 v171, v211, v169
	v_mfma_f32_16x16x32_bf16 v[160:163], v[236:239], v[88:91], v[160:163]
	v_mul_f32_e32 v164, 0x3e0293ee, v164
	v_mul_f32_e32 v165, 0x3e0293ee, v165
	v_mul_f32_e32 v166, 0x3e0293ee, v166
	s_waitcnt lgkmcnt(0)
	v_max_f32_e32 v171, v171, v171
	v_max_f32_e32 v169, v169, v171
	ds_bpermute_b32 v171, v212, v169
	s_nop 0
	v_mul_f32_e32 v160, 0x3e0293ee, v160
	v_mul_f32_e32 v161, 0x3e0293ee, v161
	v_mul_f32_e32 v162, 0x3e0293ee, v162
	v_mul_f32_e32 v167, 0x3e0293ee, v167
	s_waitcnt lgkmcnt(0)
	v_max3_f32 v231, v181, v169, v171
	v_sub_f32_e32 v156, v156, v231
	v_sub_f32_e32 v168, v168, v231
	v_exp_f32_e32 v169, v156
	v_sub_f32_e32 v156, v183, v231
	v_exp_f32_e32 v171, v168
	v_exp_f32_e32 v183, v156
	v_sub_f32_e32 v156, v157, v231
	v_add_u32_e32 v168, s70, v215
	v_sub_f32_e32 v182, v181, v231
	v_exp_f32_e32 v181, v156
	v_sub_f32_e32 v156, v170, v231
	v_add_u32_e32 v170, 0x80, v168
	v_cmp_gt_u32_e64 s[0:1], s44, v170
	v_add_u32_e32 v170, 0x70, v168
	v_exp_f32_e32 v192, v182
	s_and_b64 vcc, s[0:1], vcc
	v_cmp_gt_u32_e64 s[0:1], s44, v170
	v_add_u32_e32 v182, 0x7f, v168
	s_and_b64 s[0:1], s[0:1], s[22:23]
	v_cndmask_b32_e32 v170, v226, v164, vcc
	v_cmp_gt_u32_e32 vcc, s44, v182
	v_add_u32_e32 v182, 0x6f, v168
	v_cndmask_b32_e64 v160, v226, v160, s[0:1]
	v_cmp_gt_u32_e64 s[0:1], s44, v182
	s_and_b64 vcc, vcc, s[24:25]
	s_and_b64 s[0:1], s[0:1], s[26:27]
	v_cndmask_b32_e32 v165, v226, v165, vcc
	v_cndmask_b32_e64 v161, v226, v161, s[0:1]
	v_max_f32_e32 v164, v170, v160
	v_max_f32_e32 v182, v165, v161
	v_max3_f32 v164, v164, s45, v182
	v_add_u32_e32 v182, 0x7e, v168
	v_cmp_gt_u32_e32 vcc, s44, v182
	v_add_u32_e32 v182, 0x6e, v168
	v_exp_f32_e32 v187, v156
	v_sub_f32_e32 v156, v158, v231
	v_cmp_gt_u32_e64 s[0:1], s44, v182
	v_exp_f32_e32 v185, v156
	v_sub_f32_e32 v156, v184, v231
	s_and_b64 vcc, vcc, s[28:29]
	s_and_b64 s[0:1], s[0:1], s[30:31]
	v_add_u32_e32 v184, 0x7d, v168
	v_add_u32_e32 v168, 0x6d, v168
	v_cndmask_b32_e32 v166, v226, v166, vcc
	v_cndmask_b32_e64 v162, v226, v162, s[0:1]
	v_cmp_gt_u32_e32 vcc, s44, v184
	v_cmp_gt_u32_e64 s[0:1], s44, v168
	s_and_b64 vcc, vcc, s[34:35]
	s_and_b64 s[0:1], s[0:1], s[36:37]
	v_mul_f32_e32 v163, 0x3e0293ee, v163
	v_cndmask_b32_e32 v167, v226, v167, vcc
	v_cndmask_b32_e64 v163, v226, v163, s[0:1]
	v_max_f32_e32 v182, v166, v162
	v_max_f32_e32 v168, v167, v163
	v_max3_f32 v164, v164, v182, v168
	ds_bpermute_b32 v168, v211, v164
	v_exp_f32_e32 v191, v156
	v_sub_f32_e32 v156, v159, v231
	v_exp_f32_e32 v189, v156
	v_cvt_pk_bf16_f32 v156, v171, v183
	s_waitcnt lgkmcnt(0)
	v_max_f32_e32 v168, v168, v168
	v_max_f32_e32 v164, v164, v168
	ds_bpermute_b32 v168, v212, v164
	v_cvt_pk_bf16_f32 v157, v187, v191
	v_cvt_pk_bf16_f32 v158, v169, v181
	v_cvt_pk_bf16_f32 v159, v185, v189
	v_pk_mul_f32 v[154:155], v[154:155], v[192:193] op_sel_hi:[1,0]
	s_waitcnt lgkmcnt(0)
	v_max3_f32 v164, v180, v164, v168
	v_sub_f32_e32 v168, v170, v164
	v_sub_f32_e32 v160, v160, v164
	v_exp_f32_e32 v170, v168
	v_exp_f32_e32 v168, v160
	v_sub_f32_e32 v160, v165, v164
	v_exp_f32_e32 v182, v160
	v_sub_f32_e32 v160, v161, v164
	v_sub_f32_e32 v232, v180, v164
	v_exp_f32_e32 v180, v160
	v_sub_f32_e32 v160, v166, v164
	v_exp_f32_e32 v186, v160
	v_sub_f32_e32 v160, v162, v164
	v_exp_f32_e32 v184, v160
	v_sub_f32_e32 v160, v167, v164
	v_exp_f32_e32 v190, v160
	v_sub_f32_e32 v160, v163, v164
	v_exp_f32_e32 v188, v160
	v_pk_add_f32 v[162:163], v[170:171], v[168:169]
	v_pk_add_f32 v[166:167], v[182:183], v[180:181]
	v_pk_add_f32 v[162:163], v[162:163], 0 op_sel_hi:[1,0]
	v_exp_f32_e32 v160, v232
	v_pk_add_f32 v[162:163], v[166:167], v[162:163]
	v_pk_add_f32 v[166:167], v[186:187], v[184:185]
	v_add_u32_e32 v165, 0, v230
	v_pk_add_f32 v[162:163], v[166:167], v[162:163]
	v_pk_add_f32 v[166:167], v[190:191], v[188:189]
	v_mov_b32_e32 v161, v192
	v_pk_add_f32 v[162:163], v[166:167], v[162:163]
	ds_bpermute_b32 v167, v211, v163
	ds_bpermute_b32 v166, v211, v162
	v_pk_mul_f32 v[122:123], v[122:123], v[160:161] op_sel_hi:[1,0]
	v_pk_mul_f32 v[120:121], v[120:121], v[160:161] op_sel_hi:[1,0]
	v_pk_mul_f32 v[118:119], v[118:119], v[160:161] op_sel_hi:[1,0]
	v_pk_mul_f32 v[116:117], v[116:117], v[160:161] op_sel_hi:[1,0]
	s_waitcnt lgkmcnt(0)
	v_pk_add_f32 v[162:163], v[162:163], v[166:167]
	ds_bpermute_b32 v167, v212, v163
	ds_bpermute_b32 v166, v212, v162
	v_pk_mul_f32 v[114:115], v[114:115], v[160:161] op_sel_hi:[1,0]
	v_pk_mul_f32 v[112:113], v[112:113], v[160:161] op_sel_hi:[1,0]
	v_pk_mul_f32 v[110:111], v[110:111], v[160:161] op_sel_hi:[1,0]
	v_pk_mul_f32 v[108:109], v[108:109], v[160:161] op_sel_hi:[1,0]
	s_waitcnt lgkmcnt(0)
	v_pk_add_f32 v[162:163], v[162:163], v[166:167]
	v_add_u32_e32 v166, 0x10000, v165
	v_pk_fma_f32 v[178:179], v[178:179], v[160:161], v[162:163]
	v_pk_mul_f32 v[102:103], v[102:103], v[160:161] op_sel_hi:[1,0]
	v_pk_mul_f32 v[100:101], v[100:101], v[160:161] op_sel_hi:[1,0]
	v_pk_mul_f32 v[98:99], v[98:99], v[160:161] op_sel_hi:[1,0]
	v_pk_mul_f32 v[96:97], v[96:97], v[160:161] op_sel_hi:[1,0]
	v_pk_mul_f32 v[94:95], v[94:95], v[160:161] op_sel_hi:[1,0]
	v_pk_mul_f32 v[92:93], v[92:93], v[160:161] op_sel_hi:[1,0]
	v_pk_mul_f32 v[106:107], v[106:107], v[160:161] op_sel_hi:[1,0]
	v_pk_mul_f32 v[104:105], v[104:105], v[160:161] op_sel_hi:[1,0]
	v_cvt_pk_bf16_f32 v160, v170, v182
	v_cvt_pk_bf16_f32 v161, v186, v190
	v_cvt_pk_bf16_f32 v162, v168, v180
	v_cvt_pk_bf16_f32 v163, v184, v188
	ds_read_b64_tr_b16 v[168:169], v166
	ds_read_b64_tr_b16 v[166:167], v165 offset:60928
	ds_read_b64_tr_b16 v[180:181], v165 offset:60960
	v_pk_mul_f32 v[152:153], v[152:153], v[192:193] op_sel_hi:[1,0]
	s_waitcnt lgkmcnt(1)
	v_mfma_f32_16x16x32_bf16 v[120:123], v[166:169], v[160:163], v[120:123]
	v_mul_f32_e64 v146, v146, v192
	v_mul_f32_e64 v147, v147, v192
	v_pk_mul_f32 v[144:145], v[144:145], v[192:193] op_sel_hi:[1,0]
	v_pk_mul_f32 v[142:143], v[142:143], v[192:193] op_sel_hi:[1,0]
	v_mfma_f32_16x16x32_bf16 v[152:155], v[166:169], v[156:159], v[152:155]
	v_add_u32_e32 v166, 0x10020, v165
	v_add_u32_e32 v168, 0x10040, v165
	ds_read_b64_tr_b16 v[182:183], v166
	ds_read_b64_tr_b16 v[166:167], v165 offset:60992
	ds_read_b64_tr_b16 v[168:169], v168
	s_waitcnt lgkmcnt(0)
	v_mfma_f32_16x16x32_bf16 v[144:147], v[166:169], v[156:159], v[144:147]
	v_mul_f32_e64 v140, v140, v192
	v_mul_f32_e64 v141, v141, v192
	v_pk_mul_f32 v[134:135], v[134:135], v[192:193] op_sel_hi:[1,0]
	v_pk_mul_f32 v[132:133], v[132:133], v[192:193] op_sel_hi:[1,0]
	v_mfma_f32_16x16x32_bf16 v[112:115], v[166:169], v[160:163], v[112:115]
	v_add_u32_e32 v168, 0x10060, v165
	ds_read_b64_tr_b16 v[166:167], v165 offset:61024
	ds_read_b64_tr_b16 v[168:169], v168
	s_waitcnt lgkmcnt(0)
	v_mfma_f32_16x16x32_bf16 v[140:143], v[166:169], v[156:159], v[140:143]
	v_mul_f32_e64 v130, v130, v192
	v_mul_f32_e64 v131, v131, v192
	v_pk_mul_f32 v[128:129], v[128:129], v[192:193] op_sel_hi:[1,0]
	v_pk_mul_f32 v[126:127], v[126:127], v[192:193] op_sel_hi:[1,0]
	v_mfma_f32_16x16x32_bf16 v[108:111], v[166:169], v[160:163], v[108:111]
	v_add_u32_e32 v168, 0x10080, v165
	ds_read_b64_tr_b16 v[166:167], v165 offset:61056
	ds_read_b64_tr_b16 v[168:169], v168
	s_waitcnt lgkmcnt(0)
	v_mfma_f32_16x16x32_bf16 v[132:135], v[166:169], v[156:159], v[132:135]
	v_mul_f32_e64 v124, v124, v192
	v_mul_f32_e64 v125, v125, v192
	v_pk_mul_f32 v[150:151], v[150:151], v[192:193] op_sel_hi:[1,0]
	v_pk_mul_f32 v[148:149], v[148:149], v[192:193] op_sel_hi:[1,0]
	v_mfma_f32_16x16x32_bf16 v[100:103], v[166:169], v[160:163], v[100:103]
	v_add_u32_e32 v168, 0x100a0, v165
	ds_read_b64_tr_b16 v[166:167], v165 offset:61088
	ds_read_b64_tr_b16 v[168:169], v168
	s_waitcnt lgkmcnt(0)
	v_mfma_f32_16x16x32_bf16 v[128:131], v[166:169], v[156:159], v[128:131]
	v_mul_f32_e64 v138, v138, v192
	v_mul_f32_e64 v139, v139, v192
	v_pk_mul_f32 v[136:137], v[136:137], v[192:193] op_sel_hi:[1,0]
	s_sub_i32 s70, s70, 32
	v_mfma_f32_16x16x32_bf16 v[96:99], v[166:169], v[160:163], v[96:99]
	v_add_u32_e32 v168, 0x100c0, v165
	ds_read_b64_tr_b16 v[166:167], v165 offset:61120
	ds_read_b64_tr_b16 v[168:169], v168
	s_waitcnt lgkmcnt(0)
	v_mfma_f32_16x16x32_bf16 v[124:127], v[166:169], v[156:159], v[124:127]
	v_add_u32_e32 v230, 0x2400, v230
	v_add_u32_e32 v229, 32, v229
	s_cmpk_eq_i32 s70, 0xff60
	v_mfma_f32_16x16x32_bf16 v[92:95], v[166:169], v[160:163], v[92:95]
	ds_read_b64_tr_b16 v[166:167], v165 offset:61152
	v_add_u32_e32 v165, 0x100e0, v165
	ds_read_b64_tr_b16 v[168:169], v165
	v_mfma_f32_16x16x32_bf16 v[148:151], v[180:183], v[156:159], v[148:151]
	v_mfma_f32_16x16x32_bf16 v[116:119], v[180:183], v[160:163], v[116:119]
	s_waitcnt lgkmcnt(0)
	v_mfma_f32_16x16x32_bf16 v[136:139], v[166:169], v[156:159], v[136:139]
	v_mfma_f32_16x16x32_bf16 v[104:107], v[166:169], v[160:163], v[104:107]
	s_cbranch_scc0 .LBB0_453
	s_ashr_i32 s91, s90, 31
	s_add_i32 s68, s68, s33
	s_lshl_b64 s[0:1], s[88:89], 12
	s_lshl_b64 s[22:23], s[90:91], 13
	s_add_u32 s0, s0, s38
	s_addc_u32 s1, s1, 0
	s_add_u32 s0, s0, s22
	s_addc_u32 s1, s1, s23
	v_div_scale_f32 v47, s[22:23], v179, v179, 1.0
	v_rcp_f32_e32 v64, v47
	v_or_b32_e32 v62, s68, v200
	v_mul_lo_u32 v62, v62, s57
	v_mov_b32_e32 v63, v46
	v_fma_f32 v65, -v47, v64, 1.0
	v_fmac_f32_e32 v64, v65, v64
	v_div_scale_f32 v65, vcc, 1.0, v179, 1.0
	v_mul_f32_e32 v66, v65, v64
	v_fma_f32 v67, -v47, v66, v65
	v_fmac_f32_e32 v66, v67, v64
	v_fma_f32 v47, -v47, v66, v65
	v_lshl_add_u64 v[62:63], s[0:1], 0, v[62:63]
	v_lshl_or_b32 v60, s39, 2, v1
	v_div_fmas_f32 v47, v47, v64, v66
	v_lshlrev_b64 v[66:67], 12, v[62:63]
	v_div_fixup_f32 v64, v47, v179, 1.0
	v_lshl_add_u64 v[66:67], s[86:87], 0, v[66:67]
	v_lshlrev_b32_e32 v68, 8, v60
	v_mov_b32_e32 v69, v46
	v_lshl_add_u64 v[66:67], v[66:67], 0, v[68:69]
	v_pk_mul_f32 v[70:71], v[152:153], v[64:65] op_sel_hi:[1,0]
	v_lshl_add_u64 v[66:67], v[176:177], 1, v[66:67]
	v_mbcnt_lo_u32_b32 v243, -1, 0
	v_mbcnt_hi_u32_b32 v243, -1, v243
	v_lshrrev_b32_e32 v246, 2, v243
	v_and_b32_e32 v243, 3, v243
	v_lshl_add_u32 v243, v243, 4, v246
	v_lshlrev_b32_e32 v243, 2, v243
	ds_bpermute_b32 v244, v243, v66
	ds_bpermute_b32 v245, v243, v67
	v_pk_mul_f32 v[68:69], v[154:155], v[64:65] op_sel_hi:[1,0]
	v_cvt_pk_bf16_f32 v70, v70, v71
	v_mov_b32_e32 v61, v46
	v_cvt_pk_bf16_f32 v71, v68, v69
	ds_bpermute_b32 v70, v243, v70
	ds_bpermute_b32 v71, v243, v71
	s_waitcnt lgkmcnt(0)
	global_store_dwordx2 v[244:245], v[70:71], off
	v_pk_mul_f32 v[70:71], v[64:65], v[148:149] op_sel_hi:[0,1]
	v_pk_mul_f32 v[68:69], v[64:65], v[150:151] op_sel_hi:[0,1]
	v_cvt_pk_bf16_f32 v70, v70, v71
	v_cvt_pk_bf16_f32 v71, v68, v69
	ds_bpermute_b32 v70, v243, v70
	ds_bpermute_b32 v71, v243, v71
	s_waitcnt lgkmcnt(0)
	global_store_dwordx2 v[244:245], v[70:71], off offset:32
	v_pk_mul_f32 v[70:71], v[64:65], v[144:145] op_sel_hi:[0,1]
	v_pk_mul_f32 v[68:69], v[64:65], v[146:147] op_sel_hi:[0,1]
	v_cvt_pk_bf16_f32 v70, v70, v71
	v_cvt_pk_bf16_f32 v71, v68, v69
	ds_bpermute_b32 v70, v243, v70
	ds_bpermute_b32 v71, v243, v71
	s_waitcnt lgkmcnt(0)
	global_store_dwordx2 v[244:245], v[70:71], off offset:64
	v_pk_mul_f32 v[70:71], v[64:65], v[140:141] op_sel_hi:[0,1]
	v_pk_mul_f32 v[68:69], v[64:65], v[142:143] op_sel_hi:[0,1]
	v_cvt_pk_bf16_f32 v70, v70, v71
	v_cvt_pk_bf16_f32 v71, v68, v69
	ds_bpermute_b32 v70, v243, v70
	ds_bpermute_b32 v71, v243, v71
	s_waitcnt lgkmcnt(0)
	global_store_dwordx2 v[244:245], v[70:71], off offset:96
	v_pk_mul_f32 v[70:71], v[64:65], v[132:133] op_sel_hi:[0,1]
	v_pk_mul_f32 v[68:69], v[64:65], v[134:135] op_sel_hi:[0,1]
	v_cvt_pk_bf16_f32 v70, v70, v71
	v_cvt_pk_bf16_f32 v71, v68, v69
	ds_bpermute_b32 v70, v243, v70
	ds_bpermute_b32 v71, v243, v71
	s_waitcnt lgkmcnt(0)
	global_store_dwordx2 v[244:245], v[70:71], off offset:128
	v_pk_mul_f32 v[70:71], v[64:65], v[128:129] op_sel_hi:[0,1]
	v_pk_mul_f32 v[68:69], v[64:65], v[130:131] op_sel_hi:[0,1]
	v_cvt_pk_bf16_f32 v70, v70, v71
	v_cvt_pk_bf16_f32 v71, v68, v69
	ds_bpermute_b32 v70, v243, v70
	ds_bpermute_b32 v71, v243, v71
	s_waitcnt lgkmcnt(0)
	global_store_dwordx2 v[244:245], v[70:71], off offset:160
	v_pk_mul_f32 v[68:69], v[64:65], v[126:127] op_sel_hi:[0,1]
	v_pk_mul_f32 v[70:71], v[64:65], v[124:125] op_sel_hi:[0,1]
	v_cvt_pk_bf16_f32 v70, v70, v71
	v_cvt_pk_bf16_f32 v71, v68, v69
	v_pk_mul_f32 v[68:69], v[64:65], v[138:139] op_sel_hi:[0,1]
	v_pk_mul_f32 v[64:65], v[64:65], v[136:137] op_sel_hi:[0,1]
	ds_bpermute_b32 v70, v243, v70
	ds_bpermute_b32 v71, v243, v71
	s_waitcnt lgkmcnt(0)
	global_store_dwordx2 v[244:245], v[70:71], off offset:192
	v_cvt_pk_bf16_f32 v64, v64, v65
	v_cvt_pk_bf16_f32 v65, v68, v69
	ds_bpermute_b32 v64, v243, v64
	ds_bpermute_b32 v65, v243, v65
	s_waitcnt lgkmcnt(0)
	global_store_dwordx2 v[244:245], v[64:65], off offset:224
	s_and_saveexec_b64 s[22:23], s[18:19]
	s_cbranch_execz .LBB0_456
	v_cmp_gt_f32_e32 vcc, s56, v179
	v_lshlrev_b64 v[62:63], 6, v[62:63]
	v_lshl_add_u64 v[62:63], s[72:73], 0, v[62:63]
	v_cndmask_b32_e64 v64, 0, 32, vcc
	v_ldexp_f32 v64, v179, v64
	v_log_f32_e32 v64, v64
	v_cndmask_b32_e32 v47, 0, v227, vcc
	v_lshl_add_u64 v[62:63], v[60:61], 2, v[62:63]
	v_sub_f32_e32 v47, v64, v47
	v_add_f32_e32 v47, v231, v47
	global_store_dword v[62:63], v47, off
.LBB0_456:
	s_or_b64 exec, exec, s[22:23]
	v_div_scale_f32 v64, s[22:23], v178, v178, 1.0
	v_rcp_f32_e32 v65, v64
	v_or_b32_e32 v62, s68, v213
	v_mul_lo_u32 v62, v62, s57
	v_mov_b32_e32 v63, v46
	v_fma_f32 v66, -v64, v65, 1.0
	v_fmac_f32_e32 v65, v66, v65
	v_div_scale_f32 v66, vcc, 1.0, v178, 1.0
	v_mul_f32_e32 v67, v66, v65
	v_fma_f32 v68, -v64, v67, v66
	v_fmac_f32_e32 v67, v68, v65
	v_fma_f32 v64, -v64, v67, v66
	v_lshl_add_u64 v[62:63], s[0:1], 0, v[62:63]
	v_lshlrev_b32_e32 v47, 7, v60
	v_div_fmas_f32 v64, v64, v65, v67
	v_lshlrev_b64 v[66:67], 12, v[62:63]
	v_div_fixup_f32 v64, v64, v178, 1.0
	v_lshl_add_u64 v[66:67], s[86:87], 0, v[66:67]
	v_lshlrev_b32_e32 v68, 1, v47
	v_mov_b32_e32 v69, v46
	v_lshl_add_u64 v[66:67], v[66:67], 0, v[68:69]
	v_pk_mul_f32 v[70:71], v[120:121], v[64:65] op_sel_hi:[1,0]
	v_lshl_add_u64 v[66:67], v[176:177], 1, v[66:67]
	v_mbcnt_lo_u32_b32 v243, -1, 0
	v_mbcnt_hi_u32_b32 v243, -1, v243
	v_lshrrev_b32_e32 v246, 2, v243
	v_and_b32_e32 v243, 3, v243
	v_lshl_add_u32 v243, v243, 4, v246
	v_lshlrev_b32_e32 v243, 2, v243
	ds_bpermute_b32 v244, v243, v66
	ds_bpermute_b32 v245, v243, v67
	v_pk_mul_f32 v[68:69], v[122:123], v[64:65] op_sel_hi:[1,0]
	v_cvt_pk_bf16_f32 v70, v70, v71
	s_nop 0
	v_cvt_pk_bf16_f32 v71, v68, v69
	ds_bpermute_b32 v70, v243, v70
	ds_bpermute_b32 v71, v243, v71
	s_waitcnt lgkmcnt(0)
	global_store_dwordx2 v[244:245], v[70:71], off
	v_pk_mul_f32 v[70:71], v[116:117], v[64:65] op_sel_hi:[1,0]
	v_pk_mul_f32 v[68:69], v[118:119], v[64:65] op_sel_hi:[1,0]
	v_cvt_pk_bf16_f32 v70, v70, v71
	s_nop 0
	v_cvt_pk_bf16_f32 v71, v68, v69
	ds_bpermute_b32 v70, v243, v70
	ds_bpermute_b32 v71, v243, v71
	s_waitcnt lgkmcnt(0)
	global_store_dwordx2 v[244:245], v[70:71], off offset:32
	v_pk_mul_f32 v[70:71], v[64:65], v[112:113] op_sel_hi:[0,1]
	v_pk_mul_f32 v[68:69], v[64:65], v[114:115] op_sel_hi:[0,1]
	v_cvt_pk_bf16_f32 v70, v70, v71
	v_cvt_pk_bf16_f32 v71, v68, v69
	ds_bpermute_b32 v70, v243, v70
	ds_bpermute_b32 v71, v243, v71
	s_waitcnt lgkmcnt(0)
	global_store_dwordx2 v[244:245], v[70:71], off offset:64
	v_pk_mul_f32 v[70:71], v[64:65], v[108:109] op_sel_hi:[0,1]
	v_pk_mul_f32 v[68:69], v[64:65], v[110:111] op_sel_hi:[0,1]
	v_cvt_pk_bf16_f32 v70, v70, v71
	v_cvt_pk_bf16_f32 v71, v68, v69
	ds_bpermute_b32 v70, v243, v70
	ds_bpermute_b32 v71, v243, v71
	s_waitcnt lgkmcnt(0)
	global_store_dwordx2 v[244:245], v[70:71], off offset:96
	v_pk_mul_f32 v[70:71], v[64:65], v[100:101] op_sel_hi:[0,1]
	v_pk_mul_f32 v[68:69], v[64:65], v[102:103] op_sel_hi:[0,1]
	v_cvt_pk_bf16_f32 v70, v70, v71
	v_cvt_pk_bf16_f32 v71, v68, v69
	ds_bpermute_b32 v70, v243, v70
	ds_bpermute_b32 v71, v243, v71
	s_waitcnt lgkmcnt(0)
	global_store_dwordx2 v[244:245], v[70:71], off offset:128
	v_pk_mul_f32 v[70:71], v[64:65], v[96:97] op_sel_hi:[0,1]
	v_pk_mul_f32 v[68:69], v[64:65], v[98:99] op_sel_hi:[0,1]
	v_cvt_pk_bf16_f32 v70, v70, v71
	v_cvt_pk_bf16_f32 v71, v68, v69
	ds_bpermute_b32 v70, v243, v70
	ds_bpermute_b32 v71, v243, v71
	s_waitcnt lgkmcnt(0)
	global_store_dwordx2 v[244:245], v[70:71], off offset:160
	v_pk_mul_f32 v[68:69], v[64:65], v[94:95] op_sel_hi:[0,1]
	v_pk_mul_f32 v[70:71], v[64:65], v[92:93] op_sel_hi:[0,1]
	v_cvt_pk_bf16_f32 v70, v70, v71
	v_cvt_pk_bf16_f32 v71, v68, v69
	v_pk_mul_f32 v[68:69], v[64:65], v[106:107] op_sel_hi:[0,1]
	v_pk_mul_f32 v[64:65], v[64:65], v[104:105] op_sel_hi:[0,1]
	ds_bpermute_b32 v70, v243, v70
	ds_bpermute_b32 v71, v243, v71
	s_waitcnt lgkmcnt(0)
	global_store_dwordx2 v[244:245], v[70:71], off offset:192
	v_cvt_pk_bf16_f32 v64, v64, v65
	v_cvt_pk_bf16_f32 v65, v68, v69
	ds_bpermute_b32 v64, v243, v64
	ds_bpermute_b32 v65, v243, v65
	s_waitcnt lgkmcnt(0)
	global_store_dwordx2 v[244:245], v[64:65], off offset:224
	s_and_saveexec_b64 s[0:1], s[18:19]
	s_cbranch_execz .LBB0_458
	v_cmp_gt_f32_e32 vcc, s56, v178
	v_lshlrev_b64 v[62:63], 6, v[62:63]
	v_lshl_add_u64 v[62:63], s[72:73], 0, v[62:63]
	v_cndmask_b32_e64 v64, 0, 32, vcc
	v_ldexp_f32 v64, v178, v64
	v_log_f32_e32 v64, v64
	v_cndmask_b32_e32 v47, 0, v227, vcc
	v_lshl_add_u64 v[60:61], v[60:61], 2, v[62:63]
	v_sub_f32_e32 v47, v64, v47
	v_add_f32_e32 v47, v164, v47
	global_store_dword v[60:61], v47, off
